# v41
# baseline (speedup 1.0000x reference)
.LBB0_34:
	s_or_b64 exec, exec, s[10:11]
	ds_read_b128 v[18:21], v72
	s_waitcnt vmcnt(3)
	v_cvt_pk_f16_f32 v14, v14, v15
	v_cvt_pk_f16_f32 v15, v16, v17
	v_cvt_pk_f16_f32 v16, v10, v11
	ds_read_b128 v[22:25], v71 offset:41984
	v_cvt_pk_f16_f32 v17, v12, v13
	ds_read_b128 v[10:13], v72 offset:1024
	ds_read_b128 v[26:29], v71 offset:42048
	s_waitcnt vmcnt(1)
	v_cvt_pk_f16_f32 v0, v6, v7
	v_cvt_pk_f16_f32 v1, v8, v9
	v_cvt_pk_f16_f32 v2, v2, v3
	s_waitcnt lgkmcnt(2)
	v_mfma_f32_16x16x32_f16 v[30:33], v[18:21], v[14:17], v[22:25]
	v_cvt_pk_f16_f32 v3, v4, v5
	s_add_i32 s10, s20, s12
	s_nop 0
	v_mfma_f32_16x16x32_f16 v[18:21], v[18:21], v[0:3], v[22:25]
	ds_read_b128 v[4:7], v72 offset:2048
	s_nop 1
	ds_read_b128 v[22:25], v71 offset:42112
	s_waitcnt lgkmcnt(2)
	v_exp_f32_e32 v78, v30
	v_mfma_f32_16x16x32_f16 v[34:37], v[10:13], v[14:17], v[26:29]
	v_exp_f32_e32 v79, v31
	v_exp_f32_e32 v20, v20
	v_mfma_f32_16x16x32_f16 v[8:11], v[10:13], v[0:3], v[26:29]
	ds_read_b128 v[44:47], v71 offset:42176
	s_nop 3
	v_exp_f32_e64 v80, v34 clamp
	v_exp_f32_e64 v81, v35 clamp
	ds_read_b128 v[26:29], v72 offset:3072
	s_waitcnt lgkmcnt(2)
	v_mfma_f32_16x16x32_f16 v[48:51], v[4:7], v[14:17], v[22:25]
	v_exp_f32_e64 v82, v36 clamp
	v_exp_f32_e64 v83, v37 clamp
	v_exp_f32_e32 v21, v21
	v_mfma_f32_16x16x32_f16 v[22:25], v[4:7], v[0:3], v[22:25]
	ds_read_b128 v[52:55], v72 offset:4096
	ds_read_b128 v[56:59], v71 offset:42240
	s_nop 1
	v_exp_f32_e32 v4, v48
	s_waitcnt lgkmcnt(2)
	v_mfma_f32_16x16x32_f16 v[60:63], v[26:29], v[14:17], v[44:47]
	v_exp_f32_e32 v5, v49
	v_exp_f32_e32 v48, v32
	v_exp_f32_e32 v49, v33
	v_mfma_f32_16x16x32_f16 v[26:29], v[26:29], v[0:3], v[44:47]
	ds_read_b128 v[64:67], v71 offset:42304
	v_exp_f32_e32 v6, v50
	v_exp_f32_e32 v7, v51
	ds_read_b128 v[44:47], v72 offset:5120
	s_waitcnt lgkmcnt(2)
	v_mfma_f32_16x16x32_f16 v[74:77], v[52:55], v[14:17], v[56:59]
	v_exp_f32_e32 v50, v18
	v_exp_f32_e32 v51, v19
	v_exp_f32_e32 v26, v26
	v_mfma_f32_16x16x32_f16 v[30:33], v[52:55], v[0:3], v[56:59]
	v_exp_f32_e64 v52, v8 clamp
	v_exp_f32_e64 v53, v9 clamp
	v_exp_f32_e32 v8, v22
	s_waitcnt lgkmcnt(0)
	v_mfma_f32_16x16x32_f16 v[34:37], v[44:47], v[14:17], v[64:67]
	v_exp_f32_e32 v9, v23
	v_exp_f32_e64 v22, v10 clamp
	v_exp_f32_e64 v23, v11 clamp
	v_mfma_f32_16x16x32_f16 v[44:47], v[44:47], v[0:3], v[64:67]
	v_exp_f32_e32 v10, v24
	v_exp_f32_e32 v11, v25
	s_nop 1
	v_exp_f32_e32 v12, v34
	v_exp_f32_e32 v13, v35
	v_exp_f32_e32 v18, v36
	v_exp_f32_e32 v24, v60
	v_exp_f32_e32 v25, v61
	v_exp_f32_e64 v54, v74 clamp
	v_exp_f32_e64 v55, v75 clamp
	v_exp_f32_e32 v34, v62
	v_exp_f32_e32 v35, v63
	v_exp_f32_e64 v56, v76 clamp
	v_exp_f32_e64 v57, v77 clamp
	v_exp_f32_e32 v19, v37
	v_exp_f32_e32 v27, v27
	v_exp_f32_e64 v30, v30 clamp
	v_exp_f32_e64 v31, v31 clamp
	v_exp_f32_e32 v36, v44
	v_exp_f32_e32 v37, v45
	v_exp_f32_e32 v28, v28
	v_exp_f32_e32 v29, v29
	v_exp_f32_e64 v32, v32 clamp
	v_exp_f32_e64 v33, v33 clamp
	v_exp_f32_e32 v44, v46
	v_exp_f32_e32 v45, v47
	v_pk_fma_f32 v[58:59], v[80:81], s[2:3], 1.0 op_sel_hi:[1,0,0]
	v_pk_fma_f32 v[60:61], v[82:83], s[2:3], 1.0 op_sel_hi:[1,0,0]
	v_pk_fma_f32 v[52:53], v[52:53], s[2:3], 1.0 op_sel_hi:[1,0,0]
	v_pk_fma_f32 v[22:23], v[22:23], s[2:3], 1.0 op_sel_hi:[1,0,0]
	v_pk_fma_f32 v[54:55], v[54:55], s[2:3], 1.0 op_sel_hi:[1,0,0]
	v_pk_fma_f32 v[56:57], v[56:57], s[2:3], 1.0 op_sel_hi:[1,0,0]
	v_pk_fma_f32 v[30:31], v[30:31], s[2:3], 1.0 op_sel_hi:[1,0,0]
	v_pk_fma_f32 v[32:33], v[32:33], s[2:3], 1.0 op_sel_hi:[1,0,0]
	v_pk_fma_f32 v[46:47], v[78:79], v[58:59], v[58:59]
	v_pk_fma_f32 v[48:49], v[48:49], v[60:61], v[60:61]
	v_pk_fma_f32 v[50:51], v[50:51], v[52:53], v[52:53]
	v_pk_fma_f32 v[20:21], v[20:21], v[22:23], v[22:23]
	v_pk_fma_f32 v[24:25], v[24:25], v[54:55], v[54:55]
	v_pk_fma_f32 v[34:35], v[34:35], v[56:57], v[56:57]
	v_pk_fma_f32 v[26:27], v[26:27], v[30:31], v[30:31]
	v_pk_fma_f32 v[28:29], v[28:29], v[32:33], v[32:33]
	v_pk_fma_f32 v[58:59], v[58:59], s[6:7], v[40:41] op_sel_hi:[1,0,0] neg_lo:[1,0,0] neg_hi:[1,0,0]
	v_pk_fma_f32 v[60:61], v[60:61], s[6:7], v[40:41] op_sel_hi:[1,0,0] neg_lo:[1,0,0] neg_hi:[1,0,0]
	v_pk_fma_f32 v[52:53], v[52:53], s[6:7], v[40:41] op_sel_hi:[1,0,0] neg_lo:[1,0,0] neg_hi:[1,0,0]
	v_pk_fma_f32 v[22:23], v[22:23], s[6:7], v[40:41] op_sel_hi:[1,0,0] neg_lo:[1,0,0] neg_hi:[1,0,0]
	v_pk_fma_f32 v[54:55], v[54:55], s[6:7], v[40:41] op_sel_hi:[1,0,0] neg_lo:[1,0,0] neg_hi:[1,0,0]
	v_pk_fma_f32 v[56:57], v[56:57], s[6:7], v[40:41] op_sel_hi:[1,0,0] neg_lo:[1,0,0] neg_hi:[1,0,0]
	v_pk_fma_f32 v[30:31], v[30:31], s[6:7], v[40:41] op_sel_hi:[1,0,0] neg_lo:[1,0,0] neg_hi:[1,0,0]
	v_pk_fma_f32 v[32:33], v[32:33], s[6:7], v[40:41] op_sel_hi:[1,0,0] neg_lo:[1,0,0] neg_hi:[1,0,0]
	v_pk_fma_f32 v[46:47], v[4:5], v[46:47], v[46:47]
	v_pk_fma_f32 v[48:49], v[6:7], v[48:49], v[48:49]
	v_pk_fma_f32 v[50:51], v[8:9], v[50:51], v[50:51]
	v_pk_fma_f32 v[20:21], v[10:11], v[20:21], v[20:21]
	v_pk_fma_f32 v[24:25], v[12:13], v[24:25], v[24:25]
	v_pk_fma_f32 v[34:35], v[18:19], v[34:35], v[34:35]
	v_pk_fma_f32 v[26:27], v[36:37], v[26:27], v[26:27]
	v_pk_fma_f32 v[28:29], v[44:45], v[28:29], v[28:29]
	v_rcp_f32_e64 v46, v46 clamp
	v_rcp_f32_e64 v47, v47 clamp
	v_rcp_f32_e64 v48, v48 clamp
	v_rcp_f32_e64 v49, v49 clamp
	v_rcp_f32_e64 v50, v50 clamp
	v_rcp_f32_e64 v51, v51 clamp
	v_rcp_f32_e64 v20, v20 clamp
	v_rcp_f32_e64 v21, v21 clamp
	v_rcp_f32_e64 v24, v24 clamp
	v_rcp_f32_e64 v25, v25 clamp
	v_rcp_f32_e64 v34, v34 clamp
	v_rcp_f32_e64 v35, v35 clamp
	v_rcp_f32_e64 v26, v26 clamp
	v_rcp_f32_e64 v27, v27 clamp
	v_rcp_f32_e64 v28, v28 clamp
	v_rcp_f32_e64 v29, v29 clamp
	v_pk_mul_f32 v[46:47], v[58:59], v[46:47]
	v_pk_mul_f32 v[48:49], v[60:61], v[48:49]
	v_pk_mul_f32 v[50:51], v[52:53], v[50:51]
	v_pk_mul_f32 v[20:21], v[22:23], v[20:21]
	v_pk_mul_f32 v[22:23], v[54:55], v[24:25]
	v_pk_mul_f32 v[24:25], v[56:57], v[34:35]
	v_pk_mul_f32 v[26:27], v[30:31], v[26:27]
	v_pk_mul_f32 v[28:29], v[32:33], v[28:29]
	v_pk_fma_f32 v[4:5], v[4:5], v[46:47], v[46:47]
	v_pk_fma_f32 v[6:7], v[6:7], v[48:49], v[48:49]
	v_pk_fma_f32 v[8:9], v[8:9], v[50:51], v[50:51]
	v_pk_fma_f32 v[10:11], v[10:11], v[20:21], v[20:21]
	v_pk_fma_f32 v[12:13], v[12:13], v[22:23], v[22:23]
	v_pk_fma_f32 v[18:19], v[18:19], v[24:25], v[24:25]
	v_pk_fma_f32 v[30:31], v[36:37], v[26:27], v[26:27]
	v_pk_fma_f32 v[32:33], v[44:45], v[28:29], v[28:29]
	s_nop 0
	v_pk_fma_f32 v[4:5], v[4:5], v[4:5], s[4:5] neg_lo:[1,0,0] neg_hi:[1,0,0] clamp
	v_pk_fma_f32 v[6:7], v[6:7], v[6:7], s[4:5] neg_lo:[1,0,0] neg_hi:[1,0,0] clamp
	v_pk_fma_f32 v[8:9], v[8:9], v[8:9], s[4:5] neg_lo:[1,0,0] neg_hi:[1,0,0] clamp
	v_pk_fma_f32 v[10:11], v[10:11], v[10:11], s[4:5] neg_lo:[1,0,0] neg_hi:[1,0,0] clamp
	v_pk_fma_f32 v[12:13], v[12:13], v[12:13], s[4:5] neg_lo:[1,0,0] neg_hi:[1,0,0] clamp
	v_pk_fma_f32 v[18:19], v[18:19], v[18:19], s[4:5] neg_lo:[1,0,0] neg_hi:[1,0,0] clamp
	v_pk_fma_f32 v[30:31], v[30:31], v[30:31], s[4:5] neg_lo:[1,0,0] neg_hi:[1,0,0] clamp
	s_nop 0
	v_pk_fma_f32 v[32:33], v[32:33], v[32:33], s[4:5] neg_lo:[1,0,0] neg_hi:[1,0,0] clamp
	s_nop 0
	v_pk_fma_f32 v[8:9], v[8:9], v[8:9], s[8:9] op_sel_hi:[1,1,0]
	v_pk_fma_f32 v[10:11], v[10:11], v[10:11], s[8:9] op_sel_hi:[1,1,0]
	v_pk_fma_f32 v[12:13], v[12:13], v[12:13], s[8:9] op_sel_hi:[1,1,0]
	v_pk_fma_f32 v[18:19], v[18:19], v[18:19], s[8:9] op_sel_hi:[1,1,0]
	v_pk_fma_f32 v[32:33], v[32:33], v[32:33], s[8:9] op_sel_hi:[1,1,0]
	v_pk_fma_f32 v[4:5], v[4:5], v[4:5], s[8:9] op_sel_hi:[1,1,0]
	v_pk_fma_f32 v[6:7], v[6:7], v[6:7], s[8:9] op_sel_hi:[1,1,0]
	v_pk_fma_f32 v[30:31], v[30:31], v[30:31], s[8:9] op_sel_hi:[1,1,0]
	v_pk_mul_f32 v[8:9], v[50:51], v[8:9]
	v_pk_mul_f32 v[84:85], v[20:21], v[10:11]
	v_pk_mul_f32 v[86:87], v[22:23], v[12:13]
	v_pk_mul_f32 v[10:11], v[24:25], v[18:19]
	v_pk_mul_f32 v[12:13], v[28:29], v[32:33]
	v_pk_mul_f32 v[64:65], v[46:47], v[4:5]
	v_pk_mul_f32 v[82:83], v[48:49], v[6:7]
	v_pk_mul_f32 v[20:21], v[30:31], v[26:27]
	ds_read_b128 v[4:7], v72 offset:6144
	ds_read_b128 v[22:25], v71 offset:42368
	ds_read_b128 v[26:29], v72 offset:7168
	ds_read_b128 v[30:33], v71 offset:42432
	v_cvt_pk_f16_f32 v19, v84, v85
	v_cvt_pk_f16_f32 v18, v8, v9
	v_cvt_pk_f16_f32 v20, v20, v21
	s_waitcnt lgkmcnt(2)
	v_mfma_f32_16x16x32_f16 v[34:37], v[4:7], v[14:17], v[22:25]
	v_cvt_pk_f16_f32 v21, v12, v13
	v_mfma_f32_16x16x32_f16 v[44:47], v[4:7], v[0:3], v[22:25]
	ds_read_b128 v[4:7], v72 offset:8192
	ds_read_b128 v[48:51], v71 offset:42496
	s_waitcnt lgkmcnt(2)
	v_cvt_pk_f16_f32 v22, v64, v65
	v_mfma_f32_16x16x32_f16 v[52:55], v[26:29], v[14:17], v[30:33]
	v_cvt_pk_f16_f32 v23, v82, v83
	v_cvt_pk_f16_f32 v24, v86, v87
	v_mfma_f32_16x16x32_f16 v[26:29], v[26:29], v[0:3], v[30:33]
	ds_read_b128 v[56:59], v71 offset:42560
	v_exp_f32_e32 v86, v34
	v_exp_f32_e32 v87, v35
	ds_read_b128 v[30:33], v72 offset:9216
	s_waitcnt lgkmcnt(2)
	v_mfma_f32_16x16x32_f16 v[60:63], v[4:7], v[14:17], v[48:51]
	v_exp_f32_e64 v88, v52 clamp
	v_exp_f32_e64 v89, v53 clamp
	v_exp_f32_e64 v90, v54 clamp
	v_mfma_f32_16x16x32_f16 v[48:51], v[4:7], v[0:3], v[48:51]
	ds_read_b128 v[64:67], v72 offset:10240
	ds_read_b128 v[74:77], v71 offset:42624
	s_nop 1
	v_exp_f32_e32 v4, v60
	s_waitcnt lgkmcnt(2)
	v_mfma_f32_16x16x32_f16 v[78:81], v[30:33], v[14:17], v[56:59]
	v_exp_f32_e32 v5, v61
	v_exp_f32_e32 v60, v36
	v_exp_f32_e32 v61, v37
	v_mfma_f32_16x16x32_f16 v[30:33], v[30:33], v[0:3], v[56:59]
	ds_read_b128 v[82:85], v71 offset:42688
	v_exp_f32_e64 v91, v55 clamp
	v_exp_f32_e32 v6, v62
	ds_read_b128 v[56:59], v72 offset:11264
	s_waitcnt lgkmcnt(2)
	v_mfma_f32_16x16x32_f16 v[34:37], v[64:67], v[14:17], v[74:77]
	v_exp_f32_e32 v7, v63
	v_exp_f32_e32 v8, v48
	v_exp_f32_e32 v9, v49
	v_mfma_f32_16x16x32_f16 v[52:55], v[64:67], v[0:3], v[74:77]
	v_exp_f32_e32 v44, v44
	v_exp_f32_e32 v45, v45
	v_exp_f32_e64 v26, v26 clamp
	s_waitcnt lgkmcnt(0)
	v_mfma_f32_16x16x32_f16 v[14:17], v[56:59], v[14:17], v[82:85]
	v_exp_f32_e64 v27, v27 clamp
	v_exp_f32_e32 v46, v46
	v_exp_f32_e32 v47, v47
	v_mfma_f32_16x16x32_f16 v[56:59], v[56:59], v[0:3], v[82:85]
	v_exp_f32_e64 v28, v28 clamp
	s_nop 2
	v_exp_f32_e32 v2, v14
	v_exp_f32_e32 v3, v15
	v_exp_f32_e32 v14, v16
	v_exp_f32_e32 v15, v17
	v_exp_f32_e32 v16, v30
	v_exp_f32_e32 v17, v31
	v_exp_f32_e64 v29, v29 clamp
	v_exp_f32_e32 v0, v50
	v_exp_f32_e32 v1, v51
	v_exp_f32_e32 v48, v78
	v_exp_f32_e32 v49, v79
	v_exp_f32_e64 v34, v34 clamp
	v_exp_f32_e64 v35, v35 clamp
	v_exp_f32_e32 v50, v80
	v_exp_f32_e32 v51, v81
	v_exp_f32_e64 v36, v36 clamp
	v_exp_f32_e64 v37, v37 clamp
	v_exp_f32_e64 v30, v52 clamp
	v_exp_f32_e64 v31, v53 clamp
	v_exp_f32_e32 v52, v56
	v_exp_f32_e32 v53, v57
	v_exp_f32_e32 v32, v32
	v_exp_f32_e32 v33, v33
	v_exp_f32_e64 v54, v54 clamp
	v_exp_f32_e64 v55, v55 clamp
	v_exp_f32_e32 v56, v58
	v_cvt_pk_f16_f32 v25, v10, v11
	v_exp_f32_e32 v57, v59
	v_pk_fma_f32 v[30:31], v[30:31], s[2:3], 1.0 op_sel_hi:[1,0,0]
	v_pk_fma_f32 v[10:11], v[88:89], s[2:3], 1.0 op_sel_hi:[1,0,0]
	v_pk_fma_f32 v[12:13], v[90:91], s[2:3], 1.0 op_sel_hi:[1,0,0]
	v_pk_fma_f32 v[26:27], v[26:27], s[2:3], 1.0 op_sel_hi:[1,0,0]
	v_pk_fma_f32 v[28:29], v[28:29], s[2:3], 1.0 op_sel_hi:[1,0,0]
	v_pk_fma_f32 v[34:35], v[34:35], s[2:3], 1.0 op_sel_hi:[1,0,0]
	v_pk_fma_f32 v[36:37], v[36:37], s[2:3], 1.0 op_sel_hi:[1,0,0]
	v_pk_fma_f32 v[54:55], v[54:55], s[2:3], 1.0 op_sel_hi:[1,0,0]
	v_pk_fma_f32 v[16:17], v[16:17], v[30:31], v[30:31]
	v_pk_fma_f32 v[58:59], v[86:87], v[10:11], v[10:11]
	v_pk_fma_f32 v[10:11], v[10:11], s[6:7], v[40:41] op_sel_hi:[1,0,0] neg_lo:[1,0,0] neg_hi:[1,0,0]
	v_pk_fma_f32 v[60:61], v[60:61], v[12:13], v[12:13]
	v_pk_fma_f32 v[12:13], v[12:13], s[6:7], v[40:41] op_sel_hi:[1,0,0] neg_lo:[1,0,0] neg_hi:[1,0,0]
	v_pk_fma_f32 v[44:45], v[44:45], v[26:27], v[26:27]
	v_pk_fma_f32 v[46:47], v[46:47], v[28:29], v[28:29]
	v_pk_fma_f32 v[48:49], v[48:49], v[34:35], v[34:35]
	v_pk_fma_f32 v[50:51], v[50:51], v[36:37], v[36:37]
	v_pk_fma_f32 v[32:33], v[32:33], v[54:55], v[54:55]
	v_pk_fma_f32 v[16:17], v[52:53], v[16:17], v[16:17]
	v_pk_fma_f32 v[26:27], v[26:27], s[6:7], v[40:41] op_sel_hi:[1,0,0] neg_lo:[1,0,0] neg_hi:[1,0,0]
	v_pk_fma_f32 v[28:29], v[28:29], s[6:7], v[40:41] op_sel_hi:[1,0,0] neg_lo:[1,0,0] neg_hi:[1,0,0]
	v_pk_fma_f32 v[34:35], v[34:35], s[6:7], v[40:41] op_sel_hi:[1,0,0] neg_lo:[1,0,0] neg_hi:[1,0,0]
	v_pk_fma_f32 v[36:37], v[36:37], s[6:7], v[40:41] op_sel_hi:[1,0,0] neg_lo:[1,0,0] neg_hi:[1,0,0]
	v_pk_fma_f32 v[30:31], v[30:31], s[6:7], v[40:41] op_sel_hi:[1,0,0] neg_lo:[1,0,0] neg_hi:[1,0,0]
	v_pk_fma_f32 v[54:55], v[54:55], s[6:7], v[40:41] op_sel_hi:[1,0,0] neg_lo:[1,0,0] neg_hi:[1,0,0]
	v_pk_fma_f32 v[58:59], v[4:5], v[58:59], v[58:59]
	v_pk_fma_f32 v[60:61], v[6:7], v[60:61], v[60:61]
	v_pk_fma_f32 v[44:45], v[8:9], v[44:45], v[44:45]
	v_pk_fma_f32 v[46:47], v[0:1], v[46:47], v[46:47]
	v_pk_fma_f32 v[48:49], v[2:3], v[48:49], v[48:49]
	v_pk_fma_f32 v[50:51], v[14:15], v[50:51], v[50:51]
	v_pk_fma_f32 v[32:33], v[56:57], v[32:33], v[32:33]
	v_rcp_f32_e64 v16, v16 clamp
	v_rcp_f32_e64 v17, v17 clamp
	v_rcp_f32_e64 v58, v58 clamp
	v_rcp_f32_e64 v59, v59 clamp
	v_rcp_f32_e64 v60, v60 clamp
	v_rcp_f32_e64 v61, v61 clamp
	v_rcp_f32_e64 v44, v44 clamp
	v_rcp_f32_e64 v45, v45 clamp
	v_rcp_f32_e64 v46, v46 clamp
	v_rcp_f32_e64 v47, v47 clamp
	v_rcp_f32_e64 v48, v48 clamp
	v_rcp_f32_e64 v49, v49 clamp
	v_rcp_f32_e64 v50, v50 clamp
	v_rcp_f32_e64 v51, v51 clamp
	v_rcp_f32_e64 v32, v32 clamp
	v_rcp_f32_e64 v33, v33 clamp
	v_pk_mul_f32 v[10:11], v[10:11], v[58:59]
	v_pk_mul_f32 v[12:13], v[12:13], v[60:61]
	v_pk_mul_f32 v[26:27], v[26:27], v[44:45]
	v_pk_mul_f32 v[34:35], v[34:35], v[48:49]
	v_pk_mul_f32 v[36:37], v[36:37], v[50:51]
	v_pk_mul_f32 v[28:29], v[28:29], v[46:47]
	v_pk_mul_f32 v[16:17], v[30:31], v[16:17]
	v_pk_mul_f32 v[30:31], v[54:55], v[32:33]
	v_pk_fma_f32 v[4:5], v[4:5], v[10:11], v[10:11]
	v_pk_fma_f32 v[6:7], v[6:7], v[12:13], v[12:13]
	v_pk_fma_f32 v[8:9], v[8:9], v[26:27], v[26:27]
	v_pk_fma_f32 v[2:3], v[2:3], v[34:35], v[34:35]
	v_pk_fma_f32 v[14:15], v[14:15], v[36:37], v[36:37]
	v_pk_fma_f32 v[0:1], v[0:1], v[28:29], v[28:29]
	v_pk_fma_f32 v[32:33], v[52:53], v[16:17], v[16:17]
	v_pk_fma_f32 v[44:45], v[56:57], v[30:31], v[30:31]
	s_nop 0
	v_pk_fma_f32 v[4:5], v[4:5], v[4:5], s[4:5] neg_lo:[1,0,0] neg_hi:[1,0,0] clamp
	v_pk_fma_f32 v[6:7], v[6:7], v[6:7], s[4:5] neg_lo:[1,0,0] neg_hi:[1,0,0] clamp
	v_pk_fma_f32 v[8:9], v[8:9], v[8:9], s[4:5] neg_lo:[1,0,0] neg_hi:[1,0,0] clamp
	v_pk_fma_f32 v[0:1], v[0:1], v[0:1], s[4:5] neg_lo:[1,0,0] neg_hi:[1,0,0] clamp
	v_pk_fma_f32 v[2:3], v[2:3], v[2:3], s[4:5] neg_lo:[1,0,0] neg_hi:[1,0,0] clamp
	v_pk_fma_f32 v[14:15], v[14:15], v[14:15], s[4:5] neg_lo:[1,0,0] neg_hi:[1,0,0] clamp
	v_pk_fma_f32 v[32:33], v[32:33], v[32:33], s[4:5] neg_lo:[1,0,0] neg_hi:[1,0,0] clamp
	s_nop 0
	v_pk_fma_f32 v[44:45], v[44:45], v[44:45], s[4:5] neg_lo:[1,0,0] neg_hi:[1,0,0] clamp
	s_nop 0
	v_pk_fma_f32 v[32:33], v[32:33], v[32:33], s[8:9] op_sel_hi:[1,1,0]
	v_pk_fma_f32 v[4:5], v[4:5], v[4:5], s[8:9] op_sel_hi:[1,1,0]
	v_pk_fma_f32 v[6:7], v[6:7], v[6:7], s[8:9] op_sel_hi:[1,1,0]
	v_pk_fma_f32 v[8:9], v[8:9], v[8:9], s[8:9] op_sel_hi:[1,1,0]
	v_pk_fma_f32 v[0:1], v[0:1], v[0:1], s[8:9] op_sel_hi:[1,1,0]
	v_pk_fma_f32 v[2:3], v[2:3], v[2:3], s[8:9] op_sel_hi:[1,1,0]
	v_pk_fma_f32 v[14:15], v[14:15], v[14:15], s[8:9] op_sel_hi:[1,1,0]
	v_pk_fma_f32 v[44:45], v[44:45], v[44:45], s[8:9] op_sel_hi:[1,1,0]
	v_pk_mul_f32 v[16:17], v[32:33], v[16:17]
	v_pk_mul_f32 v[52:53], v[10:11], v[4:5]
	v_pk_mul_f32 v[54:55], v[12:13], v[6:7]
	v_pk_mul_f32 v[26:27], v[26:27], v[8:9]
	v_pk_mul_f32 v[28:29], v[28:29], v[0:1]
	v_pk_mul_f32 v[56:57], v[34:35], v[2:3]
	v_pk_mul_f32 v[58:59], v[36:37], v[14:15]
	v_pk_mul_f32 v[60:61], v[30:31], v[44:45]
	s_cmp_lt_u32 s33, 8
	s_cbranch_scc1 .Lprio_half
	s_setprio 0
.Lprio_half:
	ds_read_b128 v[0:3], v72 offset:12288
	ds_read_b128 v[4:7], v71 offset:42752
	ds_read_b128 v[8:11], v72 offset:13312
	ds_read_b128 v[12:15], v72 offset:14336
	ds_read_b128 v[34:37], v72 offset:15360
	ds_read_b128 v[44:47], v71 offset:42816
	v_cvt_pk_f16_f32 v30, v52, v53
	v_cvt_pk_f16_f32 v26, v26, v27
	v_cvt_pk_f16_f32 v31, v54, v55
	s_waitcnt lgkmcnt(4)
	v_mfma_f32_16x16x32_f16 v[48:51], v[0:3], v[22:25], v[4:7]
	v_cvt_pk_f16_f32 v32, v56, v57
	v_cvt_pk_f16_f32 v33, v58, v59
	v_cvt_pk_f16_f32 v27, v28, v29
	v_mfma_f32_16x16x32_f16 v[0:3], v[0:3], v[18:21], v[4:7]
	v_cvt_pk_f16_f32 v28, v16, v17
	s_add_i32 s11, s9, s12
	s_waitcnt lgkmcnt(3)
	v_mfma_f32_16x16x32_f16 v[48:51], v[8:11], v[30:33], v[48:51]
	s_cmp_lt_i32 s11, 0x8000
	v_cvt_pk_f16_f32 v29, v60, v61
	s_cselect_b32 s10, s11, s10
	s_ashr_i32 s11, s10, 31
	v_mfma_f32_16x16x32_f16 v[52:55], v[8:11], v[26:29], v[0:3]
	ds_read_b128 v[4:7], v72 offset:17408
	ds_read_b128 v[8:11], v71 offset:42880
	s_lshl_b64 s[10:11], s[10:11], 12
	s_add_u32 s10, s10, s36
	s_addc_u32 s11, s11, s37
	ds_read_b128 v[0:3], v72 offset:16384
	s_waitcnt lgkmcnt(3)
	v_exp_f32_e32 v106, v48
	v_mfma_f32_16x16x32_f16 v[56:59], v[12:15], v[22:25], v[44:47]
	v_exp_f32_e32 v107, v49
	v_exp_f32_e32 v110, v50
	v_mfma_f32_16x16x32_f16 v[12:15], v[12:15], v[18:21], v[44:47]
	v_exp_f32_e32 v111, v51
	v_exp_f32_e32 v114, v52
	v_mfma_f32_16x16x32_f16 v[44:47], v[34:37], v[30:33], v[56:59]
	v_exp_f32_e32 v115, v53
	v_mfma_f32_16x16x32_f16 v[56:59], v[34:37], v[26:29], v[12:15]
	ds_read_b128 v[34:37], v72 offset:19456
	ds_read_b128 v[60:63], v71 offset:42944
	s_nop 4
	v_exp_f32_e64 v108, v44 clamp
	ds_read_b128 v[12:15], v72 offset:18432
	s_waitcnt lgkmcnt(3)
	v_mfma_f32_16x16x32_f16 v[64:67], v[0:3], v[22:25], v[8:11]
	v_exp_f32_e64 v109, v45 clamp
	v_mfma_f32_16x16x32_f16 v[0:3], v[0:3], v[18:21], v[8:11]
	v_exp_f32_e64 v116, v56 clamp
	v_mfma_f32_16x16x32_f16 v[64:67], v[4:7], v[30:33], v[64:67]
	v_exp_f32_e64 v59, v59 clamp
	v_mfma_f32_16x16x32_f16 v[74:77], v[4:7], v[26:29], v[0:3]
	ds_read_b128 v[78:81], v72 offset:20480
	ds_read_b128 v[82:85], v72 offset:21504
	ds_read_b128 v[86:89], v71 offset:43008
	s_waitcnt lgkmcnt(3)
	v_exp_f32_e64 v58, v58 clamp
	v_mfma_f32_16x16x32_f16 v[6:9], v[12:15], v[22:25], v[60:63]
	v_exp_f32_e64 v117, v57 clamp
	v_mfma_f32_16x16x32_f16 v[60:63], v[12:15], v[18:21], v[60:63]
	global_load_dwordx4 v[10:13], v39, s[10:11] offset:16
	global_load_dwordx4 v[14:17], v39, s[10:11]
	global_load_dwordx4 v[2:5], v39, s[10:11] offset:2064
	v_exp_f32_e64 v113, v47 clamp
	v_mfma_f32_16x16x32_f16 v[90:93], v[34:37], v[30:33], v[6:9]
	v_exp_f32_e64 v112, v46 clamp
	v_mfma_f32_16x16x32_f16 v[60:63], v[34:37], v[26:29], v[60:63]
	s_nop 1
	global_load_dwordx4 v[6:9], v39, s[10:11] offset:2048
	ds_read_b128 v[94:97], v72 offset:22528
	ds_read_b128 v[98:101], v72 offset:23552
	ds_read_b128 v[102:105], v71 offset:43072
	s_waitcnt lgkmcnt(3)
	v_exp_f32_e32 v0, v64
	v_mfma_f32_16x16x32_f16 v[44:47], v[78:81], v[22:25], v[86:89]
	v_exp_f32_e32 v1, v65
	v_exp_f32_e32 v34, v66
	v_mfma_f32_16x16x32_f16 v[48:51], v[78:81], v[18:21], v[86:89]
	v_exp_f32_e32 v35, v67
	v_exp_f32_e32 v36, v74
	v_exp_f32_e32 v37, v75
	v_mfma_f32_16x16x32_f16 v[64:67], v[82:85], v[30:33], v[44:47]
	v_exp_f32_e32 v74, v54
	v_exp_f32_e32 v75, v55
	v_exp_f32_e32 v78, v92
	v_mfma_f32_16x16x32_f16 v[50:53], v[82:85], v[26:29], v[48:51]
	v_exp_f32_e32 v44, v76
	v_exp_f32_e32 v45, v77
	v_exp_f32_e32 v76, v90
	s_waitcnt lgkmcnt(0)
	v_mfma_f32_16x16x32_f16 v[46:49], v[94:97], v[22:25], v[102:105]
	v_exp_f32_e32 v77, v91
	v_exp_f32_e64 v64, v64 clamp
	v_exp_f32_e64 v65, v65 clamp
	v_mfma_f32_16x16x32_f16 v[54:57], v[94:97], v[18:21], v[102:105]
	v_exp_f32_e32 v79, v93
	v_exp_f32_e64 v66, v66 clamp
	v_exp_f32_e64 v67, v67 clamp
	v_mfma_f32_16x16x32_f16 v[46:49], v[98:101], v[30:33], v[46:49]
	v_exp_f32_e32 v60, v60
	v_exp_f32_e32 v61, v61
	v_exp_f32_e64 v50, v50 clamp
	v_mfma_f32_16x16x32_f16 v[54:57], v[98:101], v[26:29], v[54:57]
	v_exp_f32_e64 v51, v51 clamp
	s_nop 2
	v_exp_f32_e32 v46, v46
	v_exp_f32_e32 v47, v47
	v_exp_f32_e32 v48, v48
	v_exp_f32_e32 v49, v49
	v_exp_f32_e32 v54, v54
	v_exp_f32_e32 v55, v55
	v_exp_f32_e32 v62, v62
	v_exp_f32_e32 v63, v63
	v_exp_f32_e64 v52, v52 clamp
	v_exp_f32_e64 v53, v53 clamp
	v_exp_f32_e32 v56, v56
	v_exp_f32_e32 v57, v57
	v_pk_fma_f32 v[80:81], v[108:109], s[2:3], 1.0 op_sel_hi:[1,0,0]
	v_pk_fma_f32 v[82:83], v[112:113], s[2:3], 1.0 op_sel_hi:[1,0,0]
	v_pk_fma_f32 v[84:85], v[116:117], s[2:3], 1.0 op_sel_hi:[1,0,0]
	v_pk_fma_f32 v[58:59], v[58:59], s[2:3], 1.0 op_sel_hi:[1,0,0]
	v_pk_fma_f32 v[64:65], v[64:65], s[2:3], 1.0 op_sel_hi:[1,0,0]
	v_pk_fma_f32 v[66:67], v[66:67], s[2:3], 1.0 op_sel_hi:[1,0,0]
	v_pk_fma_f32 v[50:51], v[50:51], s[2:3], 1.0 op_sel_hi:[1,0,0]
	v_pk_fma_f32 v[52:53], v[52:53], s[2:3], 1.0 op_sel_hi:[1,0,0]
	v_pk_fma_f32 v[86:87], v[106:107], v[80:81], v[80:81]
	v_pk_fma_f32 v[88:89], v[110:111], v[82:83], v[82:83]
	v_pk_fma_f32 v[90:91], v[114:115], v[84:85], v[84:85]
	v_pk_fma_f32 v[74:75], v[74:75], v[58:59], v[58:59]
	v_pk_fma_f32 v[76:77], v[76:77], v[64:65], v[64:65]
	v_pk_fma_f32 v[78:79], v[78:79], v[66:67], v[66:67]
	v_pk_fma_f32 v[60:61], v[60:61], v[50:51], v[50:51]
	v_pk_fma_f32 v[62:63], v[62:63], v[52:53], v[52:53]
	v_pk_fma_f32 v[80:81], v[80:81], s[6:7], v[40:41] op_sel_hi:[1,0,0] neg_lo:[1,0,0] neg_hi:[1,0,0]
	v_pk_fma_f32 v[82:83], v[82:83], s[6:7], v[40:41] op_sel_hi:[1,0,0] neg_lo:[1,0,0] neg_hi:[1,0,0]
	v_pk_fma_f32 v[84:85], v[84:85], s[6:7], v[40:41] op_sel_hi:[1,0,0] neg_lo:[1,0,0] neg_hi:[1,0,0]
	v_pk_fma_f32 v[58:59], v[58:59], s[6:7], v[40:41] op_sel_hi:[1,0,0] neg_lo:[1,0,0] neg_hi:[1,0,0]
	v_pk_fma_f32 v[64:65], v[64:65], s[6:7], v[40:41] op_sel_hi:[1,0,0] neg_lo:[1,0,0] neg_hi:[1,0,0]
	v_pk_fma_f32 v[66:67], v[66:67], s[6:7], v[40:41] op_sel_hi:[1,0,0] neg_lo:[1,0,0] neg_hi:[1,0,0]
	v_pk_fma_f32 v[50:51], v[50:51], s[6:7], v[40:41] op_sel_hi:[1,0,0] neg_lo:[1,0,0] neg_hi:[1,0,0]
	v_pk_fma_f32 v[52:53], v[52:53], s[6:7], v[40:41] op_sel_hi:[1,0,0] neg_lo:[1,0,0] neg_hi:[1,0,0]
	v_pk_fma_f32 v[86:87], v[0:1], v[86:87], v[86:87]
	v_pk_fma_f32 v[88:89], v[34:35], v[88:89], v[88:89]
	v_pk_fma_f32 v[90:91], v[36:37], v[90:91], v[90:91]
	v_pk_fma_f32 v[74:75], v[44:45], v[74:75], v[74:75]
	v_pk_fma_f32 v[76:77], v[46:47], v[76:77], v[76:77]
	v_pk_fma_f32 v[78:79], v[48:49], v[78:79], v[78:79]
	v_pk_fma_f32 v[60:61], v[54:55], v[60:61], v[60:61]
	v_pk_fma_f32 v[62:63], v[56:57], v[62:63], v[62:63]
	v_rcp_f32_e64 v86, v86 clamp
	v_rcp_f32_e64 v87, v87 clamp
	v_rcp_f32_e64 v88, v88 clamp
	v_rcp_f32_e64 v89, v89 clamp
	v_rcp_f32_e64 v90, v90 clamp
	v_rcp_f32_e64 v91, v91 clamp
	v_rcp_f32_e64 v74, v74 clamp
	v_rcp_f32_e64 v75, v75 clamp
	v_rcp_f32_e64 v76, v76 clamp
	v_rcp_f32_e64 v77, v77 clamp
	v_rcp_f32_e64 v78, v78 clamp
	v_rcp_f32_e64 v79, v79 clamp
	v_rcp_f32_e64 v60, v60 clamp
	v_rcp_f32_e64 v61, v61 clamp
	v_rcp_f32_e64 v62, v62 clamp
	v_rcp_f32_e64 v63, v63 clamp
	v_pk_mul_f32 v[80:81], v[80:81], v[86:87]
	v_pk_mul_f32 v[82:83], v[82:83], v[88:89]
	v_pk_mul_f32 v[84:85], v[84:85], v[90:91]
	v_pk_mul_f32 v[58:59], v[58:59], v[74:75]
	v_pk_mul_f32 v[64:65], v[64:65], v[76:77]
	v_pk_mul_f32 v[66:67], v[66:67], v[78:79]
	v_pk_mul_f32 v[50:51], v[50:51], v[60:61]
	v_pk_mul_f32 v[60:61], v[52:53], v[62:63]
	v_pk_fma_f32 v[0:1], v[0:1], v[80:81], v[80:81]
	v_pk_fma_f32 v[34:35], v[34:35], v[82:83], v[82:83]
	v_pk_fma_f32 v[36:37], v[36:37], v[84:85], v[84:85]
	v_pk_fma_f32 v[44:45], v[44:45], v[58:59], v[58:59]
	v_pk_fma_f32 v[46:47], v[46:47], v[64:65], v[64:65]
	v_pk_fma_f32 v[48:49], v[48:49], v[66:67], v[66:67]
	v_pk_fma_f32 v[52:53], v[54:55], v[50:51], v[50:51]
	v_pk_fma_f32 v[54:55], v[56:57], v[60:61], v[60:61]
	s_nop 0
	v_pk_fma_f32 v[0:1], v[0:1], v[0:1], s[4:5] neg_lo:[1,0,0] neg_hi:[1,0,0] clamp
	v_pk_fma_f32 v[34:35], v[34:35], v[34:35], s[4:5] neg_lo:[1,0,0] neg_hi:[1,0,0] clamp
	v_pk_fma_f32 v[36:37], v[36:37], v[36:37], s[4:5] neg_lo:[1,0,0] neg_hi:[1,0,0] clamp
	v_pk_fma_f32 v[44:45], v[44:45], v[44:45], s[4:5] neg_lo:[1,0,0] neg_hi:[1,0,0] clamp
	v_pk_fma_f32 v[46:47], v[46:47], v[46:47], s[4:5] neg_lo:[1,0,0] neg_hi:[1,0,0] clamp
	v_pk_fma_f32 v[48:49], v[48:49], v[48:49], s[4:5] neg_lo:[1,0,0] neg_hi:[1,0,0] clamp
	v_pk_fma_f32 v[52:53], v[52:53], v[52:53], s[4:5] neg_lo:[1,0,0] neg_hi:[1,0,0] clamp
	s_nop 0
	v_pk_fma_f32 v[54:55], v[54:55], v[54:55], s[4:5] neg_lo:[1,0,0] neg_hi:[1,0,0] clamp
	s_nop 0
	v_pk_fma_f32 v[0:1], v[0:1], v[0:1], s[8:9] op_sel_hi:[1,1,0]
	v_pk_fma_f32 v[56:57], v[34:35], v[34:35], s[8:9] op_sel_hi:[1,1,0]
	v_pk_fma_f32 v[36:37], v[36:37], v[36:37], s[8:9] op_sel_hi:[1,1,0]
	v_pk_fma_f32 v[44:45], v[44:45], v[44:45], s[8:9] op_sel_hi:[1,1,0]
	v_pk_fma_f32 v[46:47], v[46:47], v[46:47], s[8:9] op_sel_hi:[1,1,0]
	v_pk_fma_f32 v[48:49], v[48:49], v[48:49], s[8:9] op_sel_hi:[1,1,0]
	v_pk_fma_f32 v[62:63], v[52:53], v[52:53], s[8:9] op_sel_hi:[1,1,0]
	v_pk_fma_f32 v[74:75], v[54:55], v[54:55], s[8:9] op_sel_hi:[1,1,0]
	v_pk_mul_f32 v[34:35], v[80:81], v[0:1]
	v_pk_mul_f32 v[56:57], v[82:83], v[56:57]
	v_pk_mul_f32 v[36:37], v[84:85], v[36:37]
	v_pk_mul_f32 v[52:53], v[58:59], v[44:45]
	v_pk_mul_f32 v[54:55], v[64:65], v[46:47]
	v_pk_mul_f32 v[0:1], v[66:67], v[48:49]
	v_pk_mul_f32 v[46:47], v[62:63], v[50:51]
	v_pk_mul_f32 v[44:45], v[60:61], v[74:75]
	ds_read_b128 v[48:51], v72 offset:24576
	ds_read_b128 v[58:61], v71 offset:43136
	ds_read_b128 v[62:65], v72 offset:25600
	ds_read_b128 v[74:77], v72 offset:26624
	ds_read_b128 v[78:81], v72 offset:27648
	ds_read_b128 v[82:85], v71 offset:43200
	v_cvt_pk_f16_f32 v34, v34, v35
	s_waitcnt lgkmcnt(4)
	v_mfma_f32_16x16x32_f16 v[86:89], v[48:51], v[22:25], v[58:61]
	v_cvt_pk_f16_f32 v35, v56, v57
	v_mfma_f32_16x16x32_f16 v[48:51], v[48:51], v[18:21], v[58:61]
	s_waitcnt lgkmcnt(3)
	v_mfma_f32_16x16x32_f16 v[58:61], v[62:65], v[30:33], v[86:89]
	v_mfma_f32_16x16x32_f16 v[86:89], v[62:65], v[26:29], v[48:51]
	ds_read_b128 v[62:65], v72 offset:29696
	ds_read_b128 v[90:93], v71 offset:43264
	s_nop 2
	ds_read_b128 v[48:51], v72 offset:28672
	s_waitcnt lgkmcnt(3)
	v_mfma_f32_16x16x32_f16 v[94:97], v[74:77], v[22:25], v[82:85]
	v_exp_f32_e32 v120, v86
	v_mfma_f32_16x16x32_f16 v[74:77], v[74:77], v[18:21], v[82:85]
	v_exp_f32_e32 v123, v89
	v_mfma_f32_16x16x32_f16 v[82:85], v[78:81], v[30:33], v[94:97]
	v_exp_f32_e32 v122, v88
	v_mfma_f32_16x16x32_f16 v[74:77], v[78:81], v[26:29], v[74:77]
	ds_read_b128 v[78:81], v72 offset:30720
	s_nop 0
	ds_read_b128 v[94:97], v72 offset:31744
	ds_read_b128 v[98:101], v71 offset:43328
	s_waitcnt lgkmcnt(3)
	v_exp_f32_e32 v121, v87
	v_mfma_f32_16x16x32_f16 v[102:105], v[48:51], v[22:25], v[90:93]
	s_nop 0
	v_exp_f32_e64 v66, v82 clamp
	v_exp_f32_e64 v67, v83 clamp
	v_exp_f32_e64 v118, v84 clamp
	v_mfma_f32_16x16x32_f16 v[48:51], v[48:51], v[18:21], v[90:93]
	v_exp_f32_e64 v119, v85 clamp
	v_exp_f32_e64 v124, v74 clamp
	v_exp_f32_e64 v125, v75 clamp
	v_mfma_f32_16x16x32_f16 v[90:93], v[62:65], v[30:33], v[102:105]
	v_exp_f32_e64 v126, v76 clamp
	v_exp_f32_e64 v127, v77 clamp
	v_mfma_f32_16x16x32_f16 v[102:105], v[62:65], v[26:29], v[48:51]
	ds_read_b128 v[106:109], v72 offset:32768
	ds_read_b128 v[110:113], v72 offset:33792
	v_exp_f32_e32 v62, v58
	v_exp_f32_e32 v63, v59
	v_exp_f32_e32 v64, v60
	v_exp_f32_e32 v65, v61
	ds_read_b128 v[114:117], v71 offset:43392
	s_waitcnt lgkmcnt(3)
	v_mfma_f32_16x16x32_f16 v[58:61], v[78:81], v[22:25], v[98:101]
	v_exp_f32_e32 v48, v90
	v_exp_f32_e32 v49, v91
	v_mfma_f32_16x16x32_f16 v[78:81], v[78:81], v[18:21], v[98:101]
	v_exp_f32_e32 v51, v93
	v_mfma_f32_16x16x32_f16 v[82:85], v[94:97], v[30:33], v[58:61]
	v_exp_f32_e32 v50, v92
	v_mfma_f32_16x16x32_f16 v[78:81], v[94:97], v[26:29], v[78:81]
	ds_read_b128 v[86:89], v72 offset:34816
	ds_read_b128 v[90:93], v72 offset:35840
	ds_read_b128 v[94:97], v71 offset:43456
	s_waitcnt lgkmcnt(3)
	v_exp_f32_e32 v58, v102
	v_mfma_f32_16x16x32_f16 v[74:77], v[106:109], v[22:25], v[114:117]
	v_exp_f32_e32 v59, v103
	v_exp_f32_e32 v60, v104
	v_mfma_f32_16x16x32_f16 v[98:101], v[106:109], v[18:21], v[114:117]
	v_exp_f32_e32 v61, v105
	v_exp_f32_e32 v102, v82
	v_exp_f32_e32 v103, v83
	v_exp_f32_e32 v104, v84
	v_mfma_f32_16x16x32_f16 v[74:77], v[110:113], v[30:33], v[74:77]
	v_exp_f32_e32 v105, v85
	v_mfma_f32_16x16x32_f16 v[82:85], v[110:113], v[26:29], v[98:101]
	s_waitcnt lgkmcnt(0)
	v_mfma_f32_16x16x32_f16 v[18:21], v[86:89], v[18:21], v[94:97]
	s_nop 4
	v_exp_f32_e64 v106, v74 clamp
	v_exp_f32_e64 v107, v75 clamp
	v_exp_f32_e64 v108, v76 clamp
	v_exp_f32_e64 v109, v77 clamp
	v_mfma_f32_16x16x32_f16 v[74:77], v[86:89], v[22:25], v[94:97]
	v_cvt_pk_f16_f32 v22, v36, v37
	v_cvt_pk_f16_f32 v23, v52, v53
	v_cvt_pk_f16_f32 v36, v54, v55
	v_mfma_f32_16x16x32_f16 v[18:21], v[90:93], v[26:29], v[18:21]
	v_exp_f32_e32 v52, v78
	v_exp_f32_e32 v53, v79
	v_exp_f32_e64 v54, v82 clamp
	v_mfma_f32_16x16x32_f16 v[30:33], v[90:93], v[30:33], v[74:77]
	v_exp_f32_e64 v55, v83 clamp
	s_nop 2
	v_exp_f32_e32 v18, v18
	v_exp_f32_e32 v19, v19
	v_exp_f32_e32 v26, v80
	v_exp_f32_e32 v27, v81
	v_exp_f32_e32 v30, v30
	v_exp_f32_e32 v31, v31
	v_exp_f32_e32 v32, v32
	v_exp_f32_e32 v33, v33
	v_exp_f32_e64 v28, v84 clamp
	v_exp_f32_e64 v29, v85 clamp
	v_exp_f32_e32 v20, v20
	v_cvt_pk_f16_f32 v24, v46, v47
	v_cvt_pk_f16_f32 v37, v0, v1
	v_cvt_pk_f16_f32 v25, v44, v45
	v_exp_f32_e32 v21, v21
	v_pk_fma_f32 v[0:1], v[66:67], s[2:3], 1.0 op_sel_hi:[1,0,0]
	v_pk_fma_f32 v[44:45], v[118:119], s[2:3], 1.0 op_sel_hi:[1,0,0]
	v_pk_fma_f32 v[46:47], v[124:125], s[2:3], 1.0 op_sel_hi:[1,0,0]
	v_pk_fma_f32 v[56:57], v[126:127], s[2:3], 1.0 op_sel_hi:[1,0,0]
	v_pk_fma_f32 v[66:67], v[106:107], s[2:3], 1.0 op_sel_hi:[1,0,0]
	v_pk_fma_f32 v[74:75], v[108:109], s[2:3], 1.0 op_sel_hi:[1,0,0]
	v_pk_fma_f32 v[54:55], v[54:55], s[2:3], 1.0 op_sel_hi:[1,0,0]
	v_pk_fma_f32 v[28:29], v[28:29], s[2:3], 1.0 op_sel_hi:[1,0,0]
	v_pk_fma_f32 v[62:63], v[62:63], v[0:1], v[0:1]
	v_pk_fma_f32 v[64:65], v[64:65], v[44:45], v[44:45]
	v_pk_fma_f32 v[76:77], v[120:121], v[46:47], v[46:47]
	v_pk_fma_f32 v[78:79], v[122:123], v[56:57], v[56:57]
	v_pk_fma_f32 v[80:81], v[102:103], v[66:67], v[66:67]
	v_pk_fma_f32 v[82:83], v[104:105], v[74:75], v[74:75]
	v_pk_fma_f32 v[52:53], v[52:53], v[54:55], v[54:55]
	v_pk_fma_f32 v[26:27], v[26:27], v[28:29], v[28:29]
	v_pk_fma_f32 v[0:1], v[0:1], s[6:7], v[40:41] op_sel_hi:[1,0,0] neg_lo:[1,0,0] neg_hi:[1,0,0]
	v_pk_fma_f32 v[44:45], v[44:45], s[6:7], v[40:41] op_sel_hi:[1,0,0] neg_lo:[1,0,0] neg_hi:[1,0,0]
	v_pk_fma_f32 v[46:47], v[46:47], s[6:7], v[40:41] op_sel_hi:[1,0,0] neg_lo:[1,0,0] neg_hi:[1,0,0]
	v_pk_fma_f32 v[56:57], v[56:57], s[6:7], v[40:41] op_sel_hi:[1,0,0] neg_lo:[1,0,0] neg_hi:[1,0,0]
	v_pk_fma_f32 v[66:67], v[66:67], s[6:7], v[40:41] op_sel_hi:[1,0,0] neg_lo:[1,0,0] neg_hi:[1,0,0]
	v_pk_fma_f32 v[74:75], v[74:75], s[6:7], v[40:41] op_sel_hi:[1,0,0] neg_lo:[1,0,0] neg_hi:[1,0,0]
	v_pk_fma_f32 v[54:55], v[54:55], s[6:7], v[40:41] op_sel_hi:[1,0,0] neg_lo:[1,0,0] neg_hi:[1,0,0]
	v_pk_fma_f32 v[28:29], v[28:29], s[6:7], v[40:41] op_sel_hi:[1,0,0] neg_lo:[1,0,0] neg_hi:[1,0,0]
	v_pk_fma_f32 v[62:63], v[48:49], v[62:63], v[62:63]
	v_pk_fma_f32 v[64:65], v[50:51], v[64:65], v[64:65]
	v_pk_fma_f32 v[76:77], v[58:59], v[76:77], v[76:77]
	v_pk_fma_f32 v[78:79], v[60:61], v[78:79], v[78:79]
	v_pk_fma_f32 v[80:81], v[30:31], v[80:81], v[80:81]
	v_pk_fma_f32 v[82:83], v[32:33], v[82:83], v[82:83]
	v_pk_fma_f32 v[52:53], v[18:19], v[52:53], v[52:53]
	v_pk_fma_f32 v[26:27], v[20:21], v[26:27], v[26:27]
	v_rcp_f32_e64 v62, v62 clamp
	v_rcp_f32_e64 v63, v63 clamp
	v_rcp_f32_e64 v64, v64 clamp
	v_rcp_f32_e64 v65, v65 clamp
	v_rcp_f32_e64 v76, v76 clamp
	v_rcp_f32_e64 v77, v77 clamp
	v_rcp_f32_e64 v78, v78 clamp
	v_rcp_f32_e64 v79, v79 clamp
	v_rcp_f32_e64 v80, v80 clamp
	v_rcp_f32_e64 v81, v81 clamp
	v_rcp_f32_e64 v82, v82 clamp
	v_rcp_f32_e64 v83, v83 clamp
	v_rcp_f32_e64 v52, v52 clamp
	v_rcp_f32_e64 v53, v53 clamp
	v_rcp_f32_e64 v26, v26 clamp
	v_rcp_f32_e64 v27, v27 clamp
	v_pk_mul_f32 v[52:53], v[54:55], v[52:53]
	v_pk_mul_f32 v[0:1], v[0:1], v[62:63]
	v_pk_mul_f32 v[44:45], v[44:45], v[64:65]
	v_pk_mul_f32 v[46:47], v[46:47], v[76:77]
	v_pk_mul_f32 v[56:57], v[56:57], v[78:79]
	v_pk_mul_f32 v[62:63], v[66:67], v[80:81]
	v_pk_mul_f32 v[64:65], v[74:75], v[82:83]
	v_pk_mul_f32 v[26:27], v[28:29], v[26:27]
	v_pk_fma_f32 v[18:19], v[18:19], v[52:53], v[52:53]
	v_pk_fma_f32 v[28:29], v[48:49], v[0:1], v[0:1]
	v_pk_fma_f32 v[48:49], v[50:51], v[44:45], v[44:45]
	v_pk_fma_f32 v[50:51], v[58:59], v[46:47], v[46:47]
	v_pk_fma_f32 v[54:55], v[60:61], v[56:57], v[56:57]
	v_pk_fma_f32 v[30:31], v[30:31], v[62:63], v[62:63]
	v_pk_fma_f32 v[32:33], v[32:33], v[64:65], v[64:65]
	v_pk_fma_f32 v[20:21], v[20:21], v[26:27], v[26:27]
	s_nop 0
	v_pk_fma_f32 v[28:29], v[28:29], v[28:29], s[4:5] neg_lo:[1,0,0] neg_hi:[1,0,0] clamp
	v_pk_fma_f32 v[48:49], v[48:49], v[48:49], s[4:5] neg_lo:[1,0,0] neg_hi:[1,0,0] clamp
	v_pk_fma_f32 v[50:51], v[50:51], v[50:51], s[4:5] neg_lo:[1,0,0] neg_hi:[1,0,0] clamp
	v_pk_fma_f32 v[54:55], v[54:55], v[54:55], s[4:5] neg_lo:[1,0,0] neg_hi:[1,0,0] clamp
	v_pk_fma_f32 v[30:31], v[30:31], v[30:31], s[4:5] neg_lo:[1,0,0] neg_hi:[1,0,0] clamp
	v_pk_fma_f32 v[32:33], v[32:33], v[32:33], s[4:5] neg_lo:[1,0,0] neg_hi:[1,0,0] clamp
	v_pk_fma_f32 v[18:19], v[18:19], v[18:19], s[4:5] neg_lo:[1,0,0] neg_hi:[1,0,0] clamp
	s_nop 0
	v_pk_fma_f32 v[20:21], v[20:21], v[20:21], s[4:5] neg_lo:[1,0,0] neg_hi:[1,0,0] clamp
	s_nop 0
	v_pk_fma_f32 v[28:29], v[28:29], v[28:29], s[8:9] op_sel_hi:[1,1,0]
	v_pk_fma_f32 v[48:49], v[48:49], v[48:49], s[8:9] op_sel_hi:[1,1,0]
	v_pk_fma_f32 v[50:51], v[50:51], v[50:51], s[8:9] op_sel_hi:[1,1,0]
	v_pk_fma_f32 v[54:55], v[54:55], v[54:55], s[8:9] op_sel_hi:[1,1,0]
	v_pk_fma_f32 v[30:31], v[30:31], v[30:31], s[8:9] op_sel_hi:[1,1,0]
	v_pk_fma_f32 v[32:33], v[32:33], v[32:33], s[8:9] op_sel_hi:[1,1,0]
	v_pk_fma_f32 v[18:19], v[18:19], v[18:19], s[8:9] op_sel_hi:[1,1,0]
	v_pk_fma_f32 v[20:21], v[20:21], v[20:21], s[8:9] op_sel_hi:[1,1,0]
	v_pk_mul_f32 v[0:1], v[0:1], v[28:29]
	v_pk_mul_f32 v[58:59], v[44:45], v[48:49]
	v_pk_mul_f32 v[60:61], v[46:47], v[50:51]
	v_pk_mul_f32 v[54:55], v[56:57], v[54:55]
	v_pk_mul_f32 v[62:63], v[62:63], v[30:31]
	v_pk_mul_f32 v[64:65], v[64:65], v[32:33]
	v_pk_mul_f32 v[66:67], v[18:19], v[52:53]
	v_pk_mul_f32 v[74:75], v[26:27], v[20:21]
	ds_read_b128 v[18:21], v72 offset:36864
	ds_read_b128 v[30:33], v72 offset:37888
	ds_read_b128 v[26:29], v71 offset:43520
	v_cvt_pk_f16_f32 v56, v60, v61
	v_cvt_pk_f16_f32 v57, v54, v55
	v_cvt_pk_f16_f32 v54, v62, v63
	ds_read_b128 v[60:63], v71 offset:43584
	v_cvt_pk_f16_f32 v52, v0, v1
	v_cvt_pk_f16_f32 v53, v58, v59
	s_waitcnt lgkmcnt(1)
	v_mfma_f32_16x16x32_f16 v[48:51], v[18:21], v[34:37], v[26:29]
	v_cvt_pk_f16_f32 v55, v64, v65
	v_cvt_pk_f16_f32 v58, v66, v67
	v_mfma_f32_16x16x32_f16 v[18:21], v[18:21], v[22:25], v[26:29]
	ds_read_b128 v[44:47], v72 offset:40960
	s_add_i32 s12, s12, s3
	s_add_i32 s10, s20, s12
	v_cvt_pk_f16_f32 v59, v74, v75
	v_mfma_f32_16x16x32_f16 v[26:29], v[30:33], v[52:55], v[48:51]
	s_cmp_lt_i32 s10, 0x8000
	v_add_u32_e32 v38, s7, v38
	s_nop 0
	ds_read_b128 v[48:51], v72 offset:38912
	v_mfma_f32_16x16x32_f16 v[18:21], v[30:33], v[56:59], v[18:21]
	ds_read_b128 v[30:33], v72 offset:39936
	s_nop 1
	v_cvt_pk_f16_f32 v1, v28, v29
	v_cvt_pk_f16_f32 v0, v26, v27
	s_waitcnt lgkmcnt(1)
	v_mfma_f32_16x16x32_f16 v[34:37], v[48:51], v[34:37], v[60:63]
	v_pk_max_f16 v27, v1, 0
	v_cvt_pk_f16_f32 v1, v20, v21
	v_pk_max_f16 v26, v0, 0
	v_mfma_f32_16x16x32_f16 v[20:23], v[48:51], v[22:25], v[60:63]
	v_cvt_pk_f16_f32 v0, v18, v19
	v_pk_max_f16 v18, v0, 0
	s_waitcnt lgkmcnt(0)
	v_mfma_f32_16x16x32_f16 v[34:37], v[30:33], v[52:55], v[34:37]
	v_pk_max_f16 v19, v1, 0
	v_mfma_f32_16x16x32_f16 v[20:23], v[30:33], v[56:59], v[20:23]
	s_nop 6
	v_cvt_pk_f16_f32 v0, v34, v35
	v_cvt_pk_f16_f32 v1, v36, v37
	v_pk_max_f16 v28, v0, 0
	v_pk_max_f16 v29, v1, 0
	v_cvt_pk_f16_f32 v0, v20, v21
	v_cvt_pk_f16_f32 v1, v22, v23
	v_pk_max_f16 v20, v0, 0
	v_mfma_f32_16x16x32_f16 v[24:27], v[44:47], v[26:29], 0
	v_pk_max_f16 v21, v1, 0
	s_nop 1
	v_mfma_f32_16x16x32_f16 v[18:21], v[44:47], v[18:21], 0
	s_nop 7
	v_cndmask_b32_e64 v18, v24, v18, s[0:1]
	s_cbranch_scc0 .LBB0_37
